# gate/up phase: both halves run the SwiGLU epilogue together (ALIGN form), offset barrier re-created at the unit loop back edge
# speedup vs baseline: 1.0111x; 1.0054x over previous
; #define PG8_BAR __builtin_amdgcn_s_barrier()
; template <class Epi, class Sched>
; __device__ __forceinline__ void gemm_phase(LAS unsigned char* lds, const Sched& S, const Epi& E) {
;     ...
;         if constexpr (Epi::ALIGN) { if (wr == 0) PG8_BAR; }
;         E(acc, cur, wr, wc, fr, fq, b1, bxw);
.LBB0_1248:
	s_cmpk_gt_u32 s47, 0xff
	s_cbranch_scc1 .Lp5_al
	s_barrier

; #define PG8_BAR __builtin_amdgcn_s_barrier()
; template <class Epi, class Sched>
; __device__ __forceinline__ void gemm_phase(LAS unsigned char* lds, const Sched& S, const Epi& E) {
;     ...
;         if (!has_next) break;
; #pragma unroll
;         for (int a = 0; a < 2; ++a)
; #pragma unroll
;             for (int b = 0; b < 2; ++b)
; #pragma unroll
;                 for (int m = 0; m < 4; ++m)
; #pragma unroll
;                     for (int n = 0; n < 2; ++n) acc[a][b][m][n] = (f32x4){0.f, 0.f, 0.f, 0.f};
;         cur = nxt; cA = nA; cB = nB; ++ui;
;         b1 = E.pre(cur, wc, lane);
;         if constexpr (Sched::GATHER) { PG8_GIDX(vg, cur); }
;         if constexpr (Epi::ALIGN) { if (wr == 1) PG8_BAR; }
;     }
;     if constexpr (!Epi::ALIGN) { if (wr == 0) PG8_BAR; }
.LBB0_1250:
	s_andn2_b64 vcc, exec, s[18:19]
	s_cbranch_vccz .LBB0_1163
	s_cmpk_gt_u32 s47, 0xff
	s_cbranch_scc0 .LBB0_1229
	s_barrier
	s_branch .LBB0_1229
